# P3 filter tile: w1 staging loads batched, MLP layer loops software-pipelined over two LDS operand register sets, A-fragment reads issued one segment ahead
# speedup vs baseline: 1.0024x; 1.0024x over previous
.LBB0_372:
	v_mov_b64_e32 v[2:3], v[122:123]
	global_load_dword v5, v[2:3], off
	global_load_dword v208, v[2:3], off offset:2048
	v_lshl_add_u64 v[2:3], v[2:3], 0, s[28:29]
	v_lshl_add_u64 v[2:3], v[2:3], 0, s[28:29]
	global_load_dword v209, v[2:3], off
	global_load_dword v210, v[2:3], off offset:2048
	v_lshl_add_u64 v[2:3], v[2:3], 0, s[28:29]
	v_lshl_add_u64 v[2:3], v[2:3], 0, s[28:29]
	v_add_u32_e32 v1, 0x800, v139
	v_cmp_ge_u32_e32 vcc, s33, v1
	s_and_saveexec_b64 s[6:7], vcc
	global_load_dword v211, v[2:3], off
	s_mov_b64 exec, s[6:7]
	s_waitcnt vmcnt(0)
	ds_write_b32 v138, v5
	ds_write_b32 v138, v208 offset:2048
	ds_write_b32 v138, v209 offset:4096
	ds_write_b32 v138, v210 offset:6144
	s_and_saveexec_b64 s[6:7], vcc
	ds_write_b32 v138, v211 offset:8192
	s_mov_b64 exec, s[6:7]
	global_load_dword v1, v[108:109], off
	global_load_dword v2, v[108:109], off offset:2048
	global_load_dword v3, v[110:111], off
	global_load_dword v4, v[112:113], off
	global_load_dword v5, v[114:115], off
	global_load_dword v6, v[116:117], off
	global_load_dword v7, v[118:119], off
	s_waitcnt vmcnt(5)
	ds_write2st64_b32 v137, v1, v2 offset0:198 offset1:206
	s_waitcnt vmcnt(3)
	ds_write2st64_b32 v137, v3, v4 offset0:214 offset1:222
	s_waitcnt vmcnt(1)
	ds_write2st64_b32 v137, v5, v6 offset0:230 offset1:238
	s_waitcnt vmcnt(0)
	ds_write_b32 v137, v7 offset:62976
	s_and_saveexec_b64 s[6:7], s[4:5]
	s_xor_b64 s[6:7], exec, s[6:7]
	s_cbranch_execz .LBB0_376
	global_load_dword v1, v[120:121], off
	s_waitcnt vmcnt(0)
	ds_write_b32 v137, v1 offset:65024

.LBB0_392:
	s_andn2_saveexec_b64 s[6:7], s[34:35]
	v_cvt_i32_f32_e32 v6, v5
	v_fma_f32 v7, v5, s47, |v1|
	v_fmac_f32_e32 v7, 0xb3a22168, v5
	v_fmac_f32_e32 v7, 0xa7c234c4, v5
	s_or_b64 exec, exec, s[6:7]
	v_mul_f32_e32 v3, v7, v7
	v_fmamk_f32 v4, v3, 0xb94c1982, v125
	v_fmaak_f32 v4, v3, v4, 0xbe2aaa9d
	v_mul_f32_e32 v4, v3, v4
	v_fmac_f32_e32 v7, v7, v4
	v_fmamk_f32 v4, v3, 0x37d75334, v143
	v_fmaak_f32 v4, v3, v4, 0x3d2aabf7
	v_fmaak_f32 v4, v3, v4, 0xbf000004
	v_fma_f32 v3, v3, v4, 1.0
	v_and_b32_e32 v4, 1, v6
	v_cmp_eq_u32_e64 s[6:7], 0, v4
	v_lshlrev_b32_e32 v4, 30, v6
	v_and_b32_e32 v4, 0x80000000, v4
	v_xor_b32_e32 v1, v2, v1
	v_cndmask_b32_e64 v3, v3, v7, s[6:7]
	v_xor_b32_e32 v1, v1, v4
	v_xor_b32_e32 v1, v1, v3
	v_cndmask_b32_e64 v1, v148, -v1, vcc
	ds_write_b32 v136, v1 offset:72
	s_waitcnt lgkmcnt(0)
	s_barrier
	global_load_dwordx4 v[6:9], v[64:65], off
	global_load_dwordx4 v[2:5], v[64:65], off offset:16
	s_mov_b32 s6, 0
	v_mov_b32_e32 v1, v140
	v_add_u32_e32 v14, s6, v17
	ds_read_b128 v[10:13], v1
	ds_read_b128 v[18:21], v1 offset:16
	ds_read_b32 v14, v14
	s_add_i32 s6, s6, 4
	v_add_u32_e32 v1, 0x100, v1
.LBB0_395:
	v_add_u32_e32 v216, s6, v17
	ds_read_b128 v[208:211], v1
	ds_read_b128 v[212:215], v1 offset:16
	ds_read_b32 v216, v216
	s_add_i32 s6, s6, 4
	v_add_u32_e32 v1, 0x100, v1
	s_waitcnt vmcnt(0) lgkmcnt(3)
	v_pk_fma_f32 v[6:7], v[14:15], v[10:11], v[6:7] op_sel_hi:[0,1,1]
	v_pk_fma_f32 v[8:9], v[14:15], v[12:13], v[8:9] op_sel_hi:[0,1,1]
	v_pk_fma_f32 v[2:3], v[14:15], v[18:19], v[2:3] op_sel_hi:[0,1,1]
	v_pk_fma_f32 v[4:5], v[14:15], v[20:21], v[4:5] op_sel_hi:[0,1,1]
	v_add_u32_e32 v14, s6, v17
	ds_read_b128 v[10:13], v1
	ds_read_b128 v[18:21], v1 offset:16
	ds_read_b32 v14, v14
	s_add_i32 s6, s6, 4
	v_add_u32_e32 v1, 0x100, v1
	s_waitcnt lgkmcnt(3)
	v_pk_fma_f32 v[6:7], v[216:217], v[208:209], v[6:7] op_sel_hi:[0,1,1]
	v_pk_fma_f32 v[8:9], v[216:217], v[210:211], v[8:9] op_sel_hi:[0,1,1]
	v_pk_fma_f32 v[2:3], v[216:217], v[212:213], v[2:3] op_sel_hi:[0,1,1]
	v_pk_fma_f32 v[4:5], v[216:217], v[214:215], v[4:5] op_sel_hi:[0,1,1]
	s_cmpk_eq_i32 s6, 0x84
	s_cbranch_scc0 .LBB0_395
	s_waitcnt lgkmcnt(0)
	v_pk_fma_f32 v[6:7], v[14:15], v[10:11], v[6:7] op_sel_hi:[0,1,1]
	v_pk_fma_f32 v[8:9], v[14:15], v[12:13], v[8:9] op_sel_hi:[0,1,1]
	v_pk_fma_f32 v[2:3], v[14:15], v[18:19], v[2:3] op_sel_hi:[0,1,1]
	v_pk_fma_f32 v[4:5], v[14:15], v[20:21], v[4:5] op_sel_hi:[0,1,1]
	global_load_dword v1, v[66:67], off
	s_waitcnt vmcnt(0)
	v_mul_f32_e32 v1, v6, v1
	v_and_b32_e32 v6, 0x7fffffff, v1
	v_cmp_nlt_f32_e64 s[6:7], |v1|, s37
	s_and_saveexec_b64 s[8:9], s[6:7]
	s_xor_b64 s[12:13], exec, s[8:9]
	s_cbranch_execz .LBB0_398
	v_lshrrev_b32_e32 v10, 23, v6
	v_add_u32_e32 v10, 0xffffff88, v10
	v_cmp_lt_u32_e32 vcc, 63, v10
	s_nop 1
	v_cndmask_b32_e32 v11, 0, v145, vcc
	v_add_u32_e32 v10, v11, v10
	v_cmp_lt_u32_e64 s[6:7], 31, v10
	s_nop 1
	v_cndmask_b32_e64 v11, 0, v146, s[6:7]
	v_add_u32_e32 v10, v11, v10
	v_cmp_lt_u32_e64 s[8:9], 31, v10
	s_nop 1
	v_cndmask_b32_e64 v11, 0, v146, s[8:9]
	v_add_u32_e32 v16, v11, v10
	v_and_b32_e32 v10, 0x7fffff, v6
	v_or_b32_e32 v24, 0x800000, v10
	v_mad_u64_u32 v[10:11], s[10:11], v24, s38, 0
	v_mov_b32_e32 v62, v11
	v_mad_u64_u32 v[12:13], s[10:11], v24, s39, v[62:63]
	v_mov_b32_e32 v62, v13
	v_mad_u64_u32 v[14:15], s[10:11], v24, s40, v[62:63]
	v_mov_b32_e32 v62, v15
	v_mad_u64_u32 v[18:19], s[10:11], v24, s41, v[62:63]
	v_mov_b32_e32 v62, v19
	v_mad_u64_u32 v[20:21], s[10:11], v24, s42, v[62:63]
	v_mov_b32_e32 v62, v21
	v_mad_u64_u32 v[22:23], s[10:11], v24, s43, v[62:63]
	v_mov_b32_e32 v62, v23
	v_mad_u64_u32 v[24:25], s[10:11], v24, s44, v[62:63]
	v_cndmask_b32_e32 v11, v22, v18, vcc
	v_cndmask_b32_e32 v13, v24, v20, vcc
	v_cndmask_b32_e32 v19, v25, v22, vcc
	v_cndmask_b32_e64 v15, v13, v11, s[6:7]
	v_cndmask_b32_e64 v13, v19, v13, s[6:7]
	v_cndmask_b32_e32 v19, v20, v14, vcc
	v_cndmask_b32_e64 v11, v11, v19, s[6:7]
	v_cndmask_b32_e32 v12, v18, v12, vcc
	v_cndmask_b32_e64 v13, v13, v15, s[8:9]
	v_cndmask_b32_e64 v15, v15, v11, s[8:9]
	v_sub_u32_e32 v20, 32, v16
	v_cmp_eq_u32_e64 s[10:11], 0, v16
	v_cndmask_b32_e64 v16, v19, v12, s[6:7]
	v_alignbit_b32 v21, v13, v15, v20
	v_cndmask_b32_e64 v11, v11, v16, s[8:9]
	v_cndmask_b32_e64 v13, v21, v13, s[10:11]
	v_alignbit_b32 v18, v15, v11, v20
	v_cndmask_b32_e32 v10, v14, v10, vcc
	v_cndmask_b32_e64 v15, v18, v15, s[10:11]
	v_bfe_u32 v21, v13, 29, 1
	v_cndmask_b32_e64 v10, v12, v10, s[6:7]
	v_alignbit_b32 v18, v13, v15, 30
	v_sub_u32_e32 v22, 0, v21
	v_cndmask_b32_e64 v10, v16, v10, s[8:9]
	v_xor_b32_e32 v18, v18, v22
	v_alignbit_b32 v12, v11, v10, v20
	v_cndmask_b32_e64 v11, v12, v11, s[10:11]
	v_ffbh_u32_e32 v14, v18
	v_alignbit_b32 v12, v15, v11, 30
	v_min_u32_e32 v14, 32, v14
	v_alignbit_b32 v10, v11, v10, 30
	v_xor_b32_e32 v12, v12, v22
	v_sub_u32_e32 v15, 31, v14
	v_xor_b32_e32 v10, v10, v22
	v_alignbit_b32 v16, v18, v12, v15
	v_alignbit_b32 v10, v12, v10, v15
	v_alignbit_b32 v11, v16, v10, 9
	v_ffbh_u32_e32 v12, v11
	v_min_u32_e32 v12, 32, v12
	v_lshrrev_b32_e32 v19, 29, v13
	v_not_b32_e32 v15, v12
	v_alignbit_b32 v10, v11, v10, v15
	v_lshlrev_b32_e32 v11, 31, v19
	v_or_b32_e32 v15, 0x33000000, v11
	v_add_lshl_u32 v12, v12, v14, 23
	v_lshrrev_b32_e32 v10, 9, v10
	v_sub_u32_e32 v12, v15, v12
	v_or_b32_e32 v11, 0.5, v11
	v_lshlrev_b32_e32 v14, 23, v14
	v_or_b32_e32 v10, v12, v10
	v_lshrrev_b32_e32 v12, 9, v16
	v_sub_u32_e32 v11, v11, v14
	v_or_b32_e32 v11, v12, v11
	v_mul_f32_e32 v12, 0x3fc90fda, v11
	v_fma_f32 v14, v11, s45, -v12
	v_fmac_f32_e32 v14, 0x33a22168, v11
	v_fmac_f32_e32 v14, 0x3fc90fda, v10
	v_lshrrev_b32_e32 v11, 30, v13
	v_add_f32_e32 v10, v12, v14
	v_add_u32_e32 v11, v21, v11

.LBB0_426:
	s_andn2_saveexec_b64 s[6:7], s[12:13]
	v_mul_f32_e64 v3, |v1|, s46
	v_rndne_f32_e32 v5, v3
	v_cvt_i32_f32_e32 v3, v5
	v_fma_f32 v4, v5, s47, |v1|
	v_fmac_f32_e32 v4, 0xb3a22168, v5
	v_fmac_f32_e32 v4, 0xa7c234c4, v5
	s_or_b64 exec, exec, s[6:7]
	v_mul_f32_e32 v5, v4, v4
	v_fmamk_f32 v6, v5, 0xb94c1982, v125
	v_fmaak_f32 v6, v5, v6, 0xbe2aaa9d
	v_mul_f32_e32 v6, v5, v6
	v_fmac_f32_e32 v4, v4, v6
	v_fmamk_f32 v6, v5, 0x37d75334, v143
	v_fmaak_f32 v6, v5, v6, 0x3d2aabf7
	v_fmaak_f32 v6, v5, v6, 0xbf000004
	v_fma_f32 v5, v5, v6, 1.0
	v_and_b32_e32 v6, 1, v3
	v_lshlrev_b32_e32 v3, 30, v3
	v_cmp_eq_u32_e32 vcc, 0, v6
	v_and_b32_e32 v3, 0x80000000, v3
	v_xor_b32_e32 v2, v2, v1
	v_cndmask_b32_e32 v4, v5, v4, vcc
	v_xor_b32_e32 v2, v2, v3
	v_xor_b32_e32 v2, v2, v4
	v_cmp_class_f32_e64 vcc, v1, s49
	s_mov_b32 s6, 0
	s_nop 0
	v_cndmask_b32_e32 v1, v147, v2, vcc
	ds_write_b32 v133, v1 offset:9244
	s_waitcnt lgkmcnt(0)
	s_barrier
	global_load_dwordx4 v[2:5], v[68:69], off offset:16
	global_load_dwordx4 v[6:9], v[68:69], off
	v_mov_b32_e32 v1, v142
	v_add_u32_e32 v14, s6, v141
	ds_read_b128 v[10:13], v1
	ds_read_b128 v[18:21], v1 offset:16
	ds_read_b32 v14, v14
	s_add_i32 s6, s6, 4
	v_add_u32_e32 v1, 0x100, v1
.LBB0_429:
	v_add_u32_e32 v216, s6, v141
	ds_read_b128 v[208:211], v1
	ds_read_b128 v[212:215], v1 offset:16
	ds_read_b32 v216, v216
	s_add_i32 s6, s6, 4
	v_add_u32_e32 v1, 0x100, v1
	s_waitcnt vmcnt(0) lgkmcnt(3)
	v_pk_fma_f32 v[6:7], v[14:15], v[10:11], v[6:7] op_sel_hi:[0,1,1]
	v_pk_fma_f32 v[8:9], v[14:15], v[12:13], v[8:9] op_sel_hi:[0,1,1]
	v_pk_fma_f32 v[2:3], v[14:15], v[18:19], v[2:3] op_sel_hi:[0,1,1]
	v_pk_fma_f32 v[4:5], v[14:15], v[20:21], v[4:5] op_sel_hi:[0,1,1]
	v_add_u32_e32 v14, s6, v141
	ds_read_b128 v[10:13], v1
	ds_read_b128 v[18:21], v1 offset:16
	ds_read_b32 v14, v14
	s_add_i32 s6, s6, 4
	v_add_u32_e32 v1, 0x100, v1
	s_waitcnt lgkmcnt(3)
	v_pk_fma_f32 v[6:7], v[216:217], v[208:209], v[6:7] op_sel_hi:[0,1,1]
	v_pk_fma_f32 v[8:9], v[216:217], v[210:211], v[8:9] op_sel_hi:[0,1,1]
	v_pk_fma_f32 v[2:3], v[216:217], v[212:213], v[2:3] op_sel_hi:[0,1,1]
	v_pk_fma_f32 v[4:5], v[216:217], v[214:215], v[4:5] op_sel_hi:[0,1,1]
	s_cmpk_eq_i32 s6, 0xfc
	s_cbranch_scc0 .LBB0_429
	v_add_u32_e32 v216, s6, v141
	ds_read_b128 v[208:211], v1
	ds_read_b128 v[212:215], v1 offset:16
	ds_read_b32 v216, v216
	s_add_i32 s6, s6, 4
	v_add_u32_e32 v1, 0x100, v1
	s_waitcnt lgkmcnt(3)
	v_pk_fma_f32 v[6:7], v[14:15], v[10:11], v[6:7] op_sel_hi:[0,1,1]
	v_pk_fma_f32 v[8:9], v[14:15], v[12:13], v[8:9] op_sel_hi:[0,1,1]
	v_pk_fma_f32 v[2:3], v[14:15], v[18:19], v[2:3] op_sel_hi:[0,1,1]
	v_pk_fma_f32 v[4:5], v[14:15], v[20:21], v[4:5] op_sel_hi:[0,1,1]
	s_waitcnt lgkmcnt(0)
	v_pk_fma_f32 v[6:7], v[216:217], v[208:209], v[6:7] op_sel_hi:[0,1,1]
	v_pk_fma_f32 v[8:9], v[216:217], v[210:211], v[8:9] op_sel_hi:[0,1,1]
	v_pk_fma_f32 v[2:3], v[216:217], v[212:213], v[2:3] op_sel_hi:[0,1,1]
	v_pk_fma_f32 v[4:5], v[216:217], v[214:215], v[4:5] op_sel_hi:[0,1,1]
	global_load_dword v1, v[70:71], off
	s_waitcnt vmcnt(0)
	v_mul_f32_e32 v1, v6, v1
	v_and_b32_e32 v6, 0x7fffffff, v1
	v_cmp_nlt_f32_e64 s[6:7], |v1|, s37
	s_and_saveexec_b64 s[8:9], s[6:7]
	s_xor_b64 s[12:13], exec, s[8:9]
	s_cbranch_execz .LBB0_432
	v_lshrrev_b32_e32 v10, 23, v6
	v_add_u32_e32 v10, 0xffffff88, v10
	v_cmp_lt_u32_e32 vcc, 63, v10
	s_nop 1
	v_cndmask_b32_e32 v11, 0, v145, vcc
	v_add_u32_e32 v10, v11, v10
	v_cmp_lt_u32_e64 s[6:7], 31, v10
	s_nop 1
	v_cndmask_b32_e64 v11, 0, v146, s[6:7]
	v_add_u32_e32 v10, v11, v10
	v_cmp_lt_u32_e64 s[8:9], 31, v10
	s_nop 1
	v_cndmask_b32_e64 v11, 0, v146, s[8:9]
	v_add_u32_e32 v16, v11, v10
	v_and_b32_e32 v10, 0x7fffff, v6
	v_or_b32_e32 v24, 0x800000, v10
	v_mad_u64_u32 v[10:11], s[10:11], v24, s38, 0
	v_mov_b32_e32 v62, v11
	v_mad_u64_u32 v[12:13], s[10:11], v24, s39, v[62:63]
	v_mov_b32_e32 v62, v13
	v_mad_u64_u32 v[14:15], s[10:11], v24, s40, v[62:63]
	v_mov_b32_e32 v62, v15
	v_mad_u64_u32 v[18:19], s[10:11], v24, s41, v[62:63]
	v_mov_b32_e32 v62, v19
	v_mad_u64_u32 v[20:21], s[10:11], v24, s42, v[62:63]
	v_mov_b32_e32 v62, v21
	v_mad_u64_u32 v[22:23], s[10:11], v24, s43, v[62:63]
	v_mov_b32_e32 v62, v23
	v_mad_u64_u32 v[24:25], s[10:11], v24, s44, v[62:63]
	v_cndmask_b32_e32 v11, v22, v18, vcc
	v_cndmask_b32_e32 v13, v24, v20, vcc
	v_cndmask_b32_e32 v19, v25, v22, vcc
	v_cndmask_b32_e64 v15, v13, v11, s[6:7]
	v_cndmask_b32_e64 v13, v19, v13, s[6:7]
	v_cndmask_b32_e32 v19, v20, v14, vcc
	v_cndmask_b32_e64 v11, v11, v19, s[6:7]
	v_cndmask_b32_e32 v12, v18, v12, vcc
	v_cndmask_b32_e64 v13, v13, v15, s[8:9]
	v_cndmask_b32_e64 v15, v15, v11, s[8:9]
	v_sub_u32_e32 v20, 32, v16
	v_cmp_eq_u32_e64 s[10:11], 0, v16
	v_cndmask_b32_e64 v16, v19, v12, s[6:7]
	v_alignbit_b32 v21, v13, v15, v20
	v_cndmask_b32_e64 v11, v11, v16, s[8:9]
	v_cndmask_b32_e64 v13, v21, v13, s[10:11]
	v_alignbit_b32 v18, v15, v11, v20
	v_cndmask_b32_e32 v10, v14, v10, vcc
	v_cndmask_b32_e64 v15, v18, v15, s[10:11]
	v_bfe_u32 v21, v13, 29, 1
	v_cndmask_b32_e64 v10, v12, v10, s[6:7]
	v_alignbit_b32 v18, v13, v15, 30
	v_sub_u32_e32 v22, 0, v21
	v_cndmask_b32_e64 v10, v16, v10, s[8:9]
	v_xor_b32_e32 v18, v18, v22
	v_alignbit_b32 v12, v11, v10, v20
	v_cndmask_b32_e64 v11, v12, v11, s[10:11]
	v_ffbh_u32_e32 v14, v18
	v_alignbit_b32 v12, v15, v11, 30
	v_min_u32_e32 v14, 32, v14
	v_alignbit_b32 v10, v11, v10, 30
	v_xor_b32_e32 v12, v12, v22
	v_sub_u32_e32 v15, 31, v14
	v_xor_b32_e32 v10, v10, v22
	v_alignbit_b32 v16, v18, v12, v15
	v_alignbit_b32 v10, v12, v10, v15
	v_alignbit_b32 v11, v16, v10, 9
	v_ffbh_u32_e32 v12, v11
	v_min_u32_e32 v12, 32, v12
	v_lshrrev_b32_e32 v19, 29, v13
	v_not_b32_e32 v15, v12
	v_alignbit_b32 v10, v11, v10, v15
	v_lshlrev_b32_e32 v11, 31, v19
	v_or_b32_e32 v15, 0x33000000, v11
	v_add_lshl_u32 v12, v12, v14, 23
	v_lshrrev_b32_e32 v10, 9, v10
	v_sub_u32_e32 v12, v15, v12
	v_or_b32_e32 v11, 0.5, v11
	v_lshlrev_b32_e32 v14, 23, v14
	v_or_b32_e32 v10, v12, v10
	v_lshrrev_b32_e32 v12, 9, v16
	v_sub_u32_e32 v11, v11, v14
	v_or_b32_e32 v11, v12, v11
	v_mul_f32_e32 v12, 0x3fc90fda, v11
	v_fma_f32 v14, v11, s45, -v12
	v_fmac_f32_e32 v14, 0x33a22168, v11
	v_fmac_f32_e32 v14, 0x3fc90fda, v10
	v_lshrrev_b32_e32 v11, 30, v13
	v_add_f32_e32 v10, v12, v14
	v_add_u32_e32 v11, v21, v11

.LBB0_460:
	s_andn2_saveexec_b64 s[6:7], s[12:13]
	v_mul_f32_e64 v3, |v1|, s46
	v_rndne_f32_e32 v5, v3
	v_cvt_i32_f32_e32 v3, v5
	v_fma_f32 v4, v5, s47, |v1|
	v_fmac_f32_e32 v4, 0xb3a22168, v5
	v_fmac_f32_e32 v4, 0xa7c234c4, v5
	s_or_b64 exec, exec, s[6:7]
	v_mul_f32_e32 v5, v4, v4
	v_fmamk_f32 v6, v5, 0xb94c1982, v125
	v_fmaak_f32 v6, v5, v6, 0xbe2aaa9d
	v_mul_f32_e32 v6, v5, v6
	v_fmac_f32_e32 v4, v4, v6
	v_fmamk_f32 v6, v5, 0x37d75334, v143
	v_fmaak_f32 v6, v5, v6, 0x3d2aabf7
	v_fmaak_f32 v6, v5, v6, 0xbf000004
	v_fma_f32 v5, v5, v6, 1.0
	v_and_b32_e32 v6, 1, v3
	v_lshlrev_b32_e32 v3, 30, v3
	v_cmp_eq_u32_e32 vcc, 0, v6
	v_and_b32_e32 v3, 0x80000000, v3
	v_xor_b32_e32 v2, v2, v1
	v_cndmask_b32_e32 v4, v5, v4, vcc
	v_xor_b32_e32 v2, v2, v3
	v_xor_b32_e32 v2, v2, v4
	v_cmp_class_f32_e64 vcc, v1, s49
	s_nop 1
	v_cndmask_b32_e32 v1, v147, v2, vcc
	ds_write_b32 v134, v1 offset:25884
	s_waitcnt lgkmcnt(0)
	s_barrier
	ds_read_b64 v[2:3], v135 offset:25856
	s_waitcnt lgkmcnt(0)
	ds_read_b64 v[218:219], v135 offset:25864
	v_cvt_pk_bf16_f32 v18, v2, v3
	s_waitcnt lgkmcnt(0)
	ds_read_b64 v[220:221], v135 offset:25872
	v_cvt_pk_bf16_f32 v19, v218, v219
	s_waitcnt lgkmcnt(0)
	ds_read_b64 v[218:219], v135 offset:25880
	v_cvt_pk_bf16_f32 v20, v220, v221
	s_waitcnt lgkmcnt(0)
	ds_read_b64 v[220:221], v135 offset:25984
	v_cvt_pk_bf16_f32 v21, v218, v219
	s_waitcnt lgkmcnt(0)
	ds_read_b64 v[218:219], v135 offset:25992
	v_cvt_pk_bf16_f32 v22, v220, v221
	s_waitcnt lgkmcnt(0)
	ds_read_b64 v[220:221], v135 offset:26000
	v_cvt_pk_bf16_f32 v23, v218, v219
	s_waitcnt lgkmcnt(0)
	ds_read_b64 v[218:219], v135 offset:26008
	v_cvt_pk_bf16_f32 v24, v220, v221
	s_waitcnt lgkmcnt(0)
	ds_read_b64 v[220:221], v135 offset:29952
	v_cvt_pk_bf16_f32 v25, v218, v219
	s_waitcnt lgkmcnt(0)
	ds_read_b64 v[218:219], v135 offset:29960
	v_cvt_pk_bf16_f32 v26, v220, v221
	s_waitcnt lgkmcnt(0)
	ds_read_b64 v[220:221], v135 offset:29968
	v_cvt_pk_bf16_f32 v27, v218, v219
	s_waitcnt lgkmcnt(0)
	ds_read_b64 v[218:219], v135 offset:29976
	v_cvt_pk_bf16_f32 v28, v220, v221
	s_waitcnt lgkmcnt(0)
	ds_read_b64 v[220:221], v135 offset:30080
	v_cvt_pk_bf16_f32 v29, v218, v219
	s_waitcnt lgkmcnt(0)
	ds_read_b64 v[218:219], v135 offset:30088
	v_cvt_pk_bf16_f32 v30, v220, v221
	s_waitcnt lgkmcnt(0)
	ds_read_b64 v[220:221], v135 offset:30096
	v_cvt_pk_bf16_f32 v31, v218, v219
	s_waitcnt lgkmcnt(0)
	ds_read_b64 v[218:219], v135 offset:30104
	v_cvt_pk_bf16_f32 v32, v220, v221
	s_waitcnt lgkmcnt(0)
	ds_read_b64 v[220:221], v135 offset:34048
	v_cvt_pk_bf16_f32 v33, v218, v219
	s_waitcnt lgkmcnt(0)
	ds_read_b64 v[218:219], v135 offset:34056
	v_cvt_pk_bf16_f32 v34, v220, v221
	s_waitcnt lgkmcnt(0)
	ds_read_b64 v[220:221], v135 offset:34064
	v_cvt_pk_bf16_f32 v35, v218, v219
	s_waitcnt lgkmcnt(0)
	ds_read_b64 v[218:219], v135 offset:34072
	v_cvt_pk_bf16_f32 v36, v220, v221
	s_waitcnt lgkmcnt(0)
	ds_read_b64 v[220:221], v135 offset:34176
	v_cvt_pk_bf16_f32 v37, v218, v219
	s_waitcnt lgkmcnt(0)
	ds_read_b64 v[218:219], v135 offset:34184
	v_cvt_pk_bf16_f32 v38, v220, v221
	s_waitcnt lgkmcnt(0)
	ds_read_b64 v[220:221], v135 offset:34192
	v_cvt_pk_bf16_f32 v39, v218, v219
	s_waitcnt lgkmcnt(0)
	ds_read_b64 v[218:219], v135 offset:34200
	v_cvt_pk_bf16_f32 v40, v220, v221
	s_waitcnt lgkmcnt(0)
	ds_read_b64 v[220:221], v135 offset:38144
	v_cvt_pk_bf16_f32 v41, v218, v219
	s_waitcnt lgkmcnt(0)
	ds_read_b64 v[218:219], v135 offset:38152
	v_cvt_pk_bf16_f32 v42, v220, v221
	s_waitcnt lgkmcnt(0)
	ds_read_b64 v[220:221], v135 offset:38160
	v_cvt_pk_bf16_f32 v43, v218, v219
	s_waitcnt lgkmcnt(0)
	ds_read_b64 v[218:219], v135 offset:38168
	v_cvt_pk_bf16_f32 v44, v220, v221
	s_waitcnt lgkmcnt(0)
	ds_read_b64 v[220:221], v135 offset:38272
	v_cvt_pk_bf16_f32 v45, v218, v219
	s_waitcnt lgkmcnt(0)
	ds_read_b64 v[218:219], v135 offset:38280
	v_cvt_pk_bf16_f32 v46, v220, v221
	s_waitcnt lgkmcnt(0)
	v_cvt_pk_bf16_f32 v47, v218, v219
	ds_read_b64 v[2:3], v135 offset:38288
	s_andn2_b64 vcc, exec, s[14:15]
	s_waitcnt lgkmcnt(0)
	ds_read_b64 v[218:219], v135 offset:38296
	v_cvt_pk_bf16_f32 v48, v2, v3
	s_waitcnt lgkmcnt(0)
	v_cvt_pk_bf16_f32 v49, v218, v219
	s_cbranch_vccnz .LBB0_371
	v_or_b32_e32 v9, s30, v106
	v_or_b32_e32 v10, 1, v9
	v_cvt_f32_i32_e32 v151, v10
	v_or_b32_e32 v10, 2, v9
	v_cvt_f32_i32_e32 v152, v10
	v_or_b32_e32 v10, 3, v9
	v_cvt_f32_i32_e32 v153, v10
	v_or_b32_e32 v10, 16, v9
	v_cvt_f32_i32_e32 v154, v10
	v_or_b32_e32 v10, 17, v9
	v_cvt_f32_i32_e32 v155, v10
	v_or_b32_e32 v10, 18, v9
	v_cvt_f32_i32_e32 v156, v10
	v_or_b32_e32 v10, 19, v9
	v_cvt_f32_i32_e32 v157, v10
	v_or_b32_e32 v10, 32, v9
	v_cvt_f32_i32_e32 v158, v10
	v_or_b32_e32 v10, 33, v9
	v_cvt_f32_i32_e32 v159, v10
	v_or_b32_e32 v10, 34, v9
	v_cvt_f32_i32_e32 v160, v10
	v_or_b32_e32 v10, 35, v9
	v_cvt_f32_i32_e32 v161, v10
	v_or_b32_e32 v10, 48, v9
	v_cvt_f32_i32_e32 v162, v10
	v_or_b32_e32 v10, 49, v9
	global_load_dword v2, v[72:73], off
	global_load_dword v1, v[74:75], off
	global_load_dword v4, v[76:77], off
	global_load_dword v3, v[78:79], off
	global_load_dword v6, v[80:81], off
	global_load_dword v5, v[82:83], off
	global_load_dword v8, v[84:85], off
	global_load_dword v7, v[86:87], off
	global_load_dword v50, v[104:105], off
	v_cvt_f32_i32_e32 v150, v9
	v_cmp_eq_u32_e64 s[6:7], 0, v9
	v_cvt_f32_i32_e32 v163, v10
	v_or_b32_e32 v10, 50, v9
	v_or_b32_e32 v9, 51, v9
	v_cvt_f32_i32_e32 v164, v10
	v_cvt_f32_i32_e32 v165, v9
	global_load_dword v10, v[88:89], off
	global_load_dword v9, v[90:91], off
	global_load_dword v12, v[92:93], off
	global_load_dword v11, v[94:95], off
	global_load_dword v14, v[96:97], off
	global_load_dword v13, v[98:99], off
	global_load_dword v16, v[100:101], off
	global_load_dword v15, v[102:103], off
	s_ashr_i32 s31, s30, 31
	v_mov_b32_e32 v166, v124
	s_mov_b64 s[8:9], s[24:25]
	s_mov_b64 s[10:11], s[22:23]
	v_mov_b64_e32 v[130:131], v[128:129]
	s_mov_b32 s52, s97
	s_branch .LBB0_465
